# each big kernel also pre-loads its own code bytes into L2 through the data path at entry (one coalesced global_load at pc+tid*64) so the I-cache warm-up hops hit L2
# speedup vs baseline: 1.3586x; 1.0459x over previous
_Z11k_localsortPKiS0_S0_PjPtPiPKjPKfS7_S7_S7_S7_S7_S7_S7_S7_S7_PDF16_S8_S8_PfS9_:
	s_getpc_b64 s[4:5]
	v_lshlrev_b32_e32 v95, 6, v0
	s_movk_i32 s6, 0xa0
	v_cmp_gt_u32_e32 vcc, s6, v0
	s_and_saveexec_b64 s[6:7], vcc
	global_load_dword v95, v95, s[4:5]
	s_mov_b64 exec, s[6:7]
	s_cmpk_lt_u32 s2, 0xde
	s_mov_b64 s[4:5], -1
	s_cbranch_scc0 .LBB1_84
	s_load_dwordx4 s[4:7], s[0:1], 0x0
	s_load_dwordx2 s[8:9], s[0:1], 0x10
	s_movk_i32 s3, 0x187
	v_cmp_gt_u32_e64 s[50:51], s3, v0
	v_lshlrev_b32_e32 v38, 2, v0
	s_and_saveexec_b64 s[10:11], s[50:51]
	v_mov_b32_e32 v1, 0
	ds_write_b32 v38, v1
	s_or_b64 exec, exec, s[10:11]
	s_mul_i32 s3, s2, 0x6f
	s_bfe_u32 s64, s3, 0x3000d
	v_mov_b32_e32 v1, 0x4a
	s_mul_i32 s3, s64, 0xffffffb6
	v_sub_co_u32_e32 v1, vcc, s2, v1
	s_add_i32 s3, s3, s2
	v_readfirstlane_b32 s10, v1
	s_cmpk_lt_u32 s10, 0x4a
	s_waitcnt lgkmcnt(0)
	s_cselect_b32 s8, s6, s8
	s_cselect_b32 s9, s7, s9
	s_and_b64 s[6:7], vcc, exec
	s_cselect_b32 s9, s5, s9
	s_cselect_b32 s8, s4, s8
	s_lshl_b32 s4, s3, 14
	s_ashr_i32 s5, s4, 31
	s_lshl_b64 s[6:7], s[4:5], 2
	s_add_u32 s6, s8, s6
	s_addc_u32 s7, s9, s7
	s_add_u32 s8, s6, 0x493e00
	s_addc_u32 s9, s7, 0
	s_sub_i32 s3, 0x124f80, s4
	s_min_i32 s3, s3, 0x4000
	s_ashr_i32 s33, s3, 2
	v_cmp_gt_i32_e32 vcc, s33, v0
	v_mov_b32_e32 v10, -1
	v_mov_b32_e32 v14, 0
	v_lshlrev_b32_e32 v34, 4, v0
	v_mov_b32_e32 v26, 0
	v_mov_b32_e32 v27, 0
	v_mov_b32_e32 v28, 0
	v_mov_b32_e32 v29, 0
	v_mov_b32_e32 v30, -1
	v_mov_b32_e32 v31, -1
	v_mov_b32_e32 v32, -1
	v_mov_b32_e32 v33, -1
	s_and_saveexec_b64 s[4:5], vcc
	s_cbranch_execz .LBB1_5
	global_load_dwordx4 v[30:33], v34, s[8:9] nt
	global_load_dwordx4 v[26:29], v34, s[6:7] nt

	.amdhsa_kernel _Z11k_localsortPKiS0_S0_PjPtPiPKjPKfS7_S7_S7_S7_S7_S7_S7_S7_S7_PDF16_S8_S8_PfS9_
		.amdhsa_group_segment_fixed_size 1696
		.amdhsa_private_segment_fixed_size 0
		.amdhsa_kernarg_size 176
		.amdhsa_user_sgpr_count 2
		.amdhsa_user_sgpr_dispatch_ptr 0
		.amdhsa_user_sgpr_queue_ptr 0
		.amdhsa_user_sgpr_kernarg_segment_ptr 1
		.amdhsa_user_sgpr_dispatch_id 0
		.amdhsa_user_sgpr_kernarg_preload_length 0
		.amdhsa_user_sgpr_kernarg_preload_offset 0
		.amdhsa_user_sgpr_private_segment_size 0
		.amdhsa_uses_dynamic_stack 0
		.amdhsa_enable_private_segment 0
		.amdhsa_system_sgpr_workgroup_id_x 1
		.amdhsa_system_sgpr_workgroup_id_y 0
		.amdhsa_system_sgpr_workgroup_id_z 0
		.amdhsa_system_sgpr_workgroup_info 0
		.amdhsa_system_vgpr_workitem_id 0
		.amdhsa_next_free_vgpr 96
		.amdhsa_next_free_sgpr 65
		.amdhsa_accum_offset 96
		.amdhsa_reserve_vcc 1
		.amdhsa_float_round_mode_32 0
		.amdhsa_float_round_mode_16_64 0
		.amdhsa_float_denorm_mode_32 3
		.amdhsa_float_denorm_mode_16_64 3
		.amdhsa_dx10_clamp 1
		.amdhsa_ieee_mode 1
		.amdhsa_fp16_overflow 0
		.amdhsa_tg_split 0
		.amdhsa_exception_fp_ieee_invalid_op 0
		.amdhsa_exception_fp_denorm_src 0
		.amdhsa_exception_fp_ieee_div_zero 0
		.amdhsa_exception_fp_ieee_overflow 0
		.amdhsa_exception_fp_ieee_underflow 0
		.amdhsa_exception_fp_ieee_inexact 0
		.amdhsa_exception_int_div_zero 0
	.end_amdhsa_kernel

_Z12k_bucketsortPKjPKtPKiPiPj:
	s_getpc_b64 s[4:5]
	v_lshlrev_b32_e32 v63, 6, v0
	s_movk_i32 s6, 0x160
	v_cmp_gt_u32_e32 vcc, s6, v0
	s_and_saveexec_b64 s[6:7], vcc
	global_load_dword v63, v63, s[4:5]
	s_mov_b64 exec, s[6:7]
	s_movk_i32 s3, 0xde
	v_cmp_gt_u32_e32 vcc, s3, v0
	v_mov_b32_e32 v5, 0
	v_mov_b32_e32 v4, 0
	s_and_saveexec_b64 s[4:5], vcc
	s_cbranch_execz .LBB2_2
	s_load_dwordx2 s[6:7], s[0:1], 0x10
	s_movk_i32 s3, 0x188
	v_mov_b32_e32 v1, s2
	v_mad_u32_u24 v2, v0, s3, v1
	v_ashrrev_i32_e32 v3, 31, v2
	s_waitcnt lgkmcnt(0)
	v_lshl_add_u64 v[2:3], v[2:3], 2, s[6:7]
	global_load_dwordx2 v[4:5], v[2:3], off
	v_lshlrev_b32_e32 v1, 2, v0
	v_add_u32_e32 v1, 0xcc00, v1
	s_waitcnt vmcnt(0)
	v_sub_u32_e32 v5, v5, v4
	ds_write2_b32 v1, v4, v5 offset1:224

	.amdhsa_kernel _Z12k_bucketsortPKjPKtPKiPiPj
		.amdhsa_group_segment_fixed_size 54160
		.amdhsa_private_segment_fixed_size 0
		.amdhsa_kernarg_size 40
		.amdhsa_user_sgpr_count 2
		.amdhsa_user_sgpr_dispatch_ptr 0
		.amdhsa_user_sgpr_queue_ptr 0
		.amdhsa_user_sgpr_kernarg_segment_ptr 1
		.amdhsa_user_sgpr_dispatch_id 0
		.amdhsa_user_sgpr_kernarg_preload_length 0
		.amdhsa_user_sgpr_kernarg_preload_offset 0
		.amdhsa_user_sgpr_private_segment_size 0
		.amdhsa_uses_dynamic_stack 0
		.amdhsa_enable_private_segment 0
		.amdhsa_system_sgpr_workgroup_id_x 1
		.amdhsa_system_sgpr_workgroup_id_y 0
		.amdhsa_system_sgpr_workgroup_id_z 0
		.amdhsa_system_sgpr_workgroup_info 0
		.amdhsa_system_vgpr_workitem_id 0
		.amdhsa_next_free_vgpr 64
		.amdhsa_next_free_sgpr 82
		.amdhsa_accum_offset 64
		.amdhsa_reserve_vcc 1
		.amdhsa_float_round_mode_32 0
		.amdhsa_float_round_mode_16_64 0
		.amdhsa_float_denorm_mode_32 3
		.amdhsa_float_denorm_mode_16_64 3
		.amdhsa_dx10_clamp 1
		.amdhsa_ieee_mode 1
		.amdhsa_fp16_overflow 0
		.amdhsa_tg_split 0
		.amdhsa_exception_fp_ieee_invalid_op 0
		.amdhsa_exception_fp_denorm_src 0
		.amdhsa_exception_fp_ieee_div_zero 0
		.amdhsa_exception_fp_ieee_overflow 0
		.amdhsa_exception_fp_ieee_underflow 0
		.amdhsa_exception_fp_ieee_inexact 0
		.amdhsa_exception_int_div_zero 0
	.end_amdhsa_kernel

_Z7k_layerILi1EEvPKDF16_PKiPKjS3_S3_S1_PKfPDF16_PhS3_S7_Pf:
	s_getpc_b64 s[4:5]
	v_lshlrev_b32_e32 v116, 6, v0
	s_movk_i32 s6, 0xd0
	v_cmp_gt_u32_e32 vcc, s6, v0
	s_and_saveexec_b64 s[6:7], vcc
	global_load_dword v116, v116, s[4:5]
	s_mov_b64 exec, s[6:7]
	v_readfirstlane_b32 s3, v0
	s_lshr_b32 s3, s3, 6
	s_cmp_eq_u32 s3, 0
	s_cbranch_scc1 .Lic1p_t0
	s_cmp_eq_u32 s3, 1
	s_cbranch_scc1 .Lic1p_t1
	s_cmp_eq_u32 s3, 2
	s_cbranch_scc1 .Lic1p_t2
	s_cmp_eq_u32 s3, 3
	s_cbranch_scc1 .Lic1p_t3
	s_cmp_eq_u32 s3, 4
	s_cbranch_scc1 .Lic1p_t4
	s_cmp_eq_u32 s3, 5
	s_cbranch_scc1 .Lic1p_t5
	s_cmp_eq_u32 s3, 6
	s_cbranch_scc1 .Lic1p_t6
	s_cmp_eq_u32 s3, 7
	s_cbranch_scc1 .Lic1p_t7
	s_cmp_eq_u32 s3, 8
	s_cbranch_scc1 .Lic1p_t8
	s_cmp_eq_u32 s3, 9
	s_cbranch_scc1 .Lic1p_t9

	.amdhsa_kernel _Z7k_layerILi1EEvPKDF16_PKiPKjS3_S3_S1_PKfPDF16_PhS3_S7_Pf
		.amdhsa_group_segment_fixed_size 35072
		.amdhsa_private_segment_fixed_size 0
		.amdhsa_kernarg_size 352
		.amdhsa_user_sgpr_count 2
		.amdhsa_user_sgpr_dispatch_ptr 0
		.amdhsa_user_sgpr_queue_ptr 0
		.amdhsa_user_sgpr_kernarg_segment_ptr 1
		.amdhsa_user_sgpr_dispatch_id 0
		.amdhsa_user_sgpr_kernarg_preload_length 0
		.amdhsa_user_sgpr_kernarg_preload_offset 0
		.amdhsa_user_sgpr_private_segment_size 0
		.amdhsa_uses_dynamic_stack 0
		.amdhsa_enable_private_segment 0
		.amdhsa_system_sgpr_workgroup_id_x 1
		.amdhsa_system_sgpr_workgroup_id_y 0
		.amdhsa_system_sgpr_workgroup_id_z 0
		.amdhsa_system_sgpr_workgroup_info 0
		.amdhsa_system_vgpr_workitem_id 0
		.amdhsa_next_free_vgpr 117
		.amdhsa_next_free_sgpr 37
		.amdhsa_accum_offset 120
		.amdhsa_reserve_vcc 1
		.amdhsa_float_round_mode_32 0
		.amdhsa_float_round_mode_16_64 0
		.amdhsa_float_denorm_mode_32 3
		.amdhsa_float_denorm_mode_16_64 3
		.amdhsa_dx10_clamp 1
		.amdhsa_ieee_mode 1
		.amdhsa_fp16_overflow 0
		.amdhsa_tg_split 0
		.amdhsa_exception_fp_ieee_invalid_op 0
		.amdhsa_exception_fp_denorm_src 0
		.amdhsa_exception_fp_ieee_div_zero 0
		.amdhsa_exception_fp_ieee_overflow 0
		.amdhsa_exception_fp_ieee_underflow 0
		.amdhsa_exception_fp_ieee_inexact 0
		.amdhsa_exception_int_div_zero 0
	.end_amdhsa_kernel

_Z7k_layerILi2EEvPKDF16_PKiPKjS3_S3_S1_PKfPDF16_PhS3_S7_Pf:
	s_getpc_b64 s[4:5]
	v_lshlrev_b32_e32 v104, 6, v0
	s_movk_i32 s6, 0xc8
	v_cmp_gt_u32_e32 vcc, s6, v0
	s_and_saveexec_b64 s[6:7], vcc
	global_load_dword v104, v104, s[4:5]
	s_mov_b64 exec, s[6:7]
	v_readfirstlane_b32 s3, v0
	s_lshr_b32 s3, s3, 6
	s_cmp_eq_u32 s3, 0
	s_cbranch_scc1 .Lic2p_t0
	s_cmp_eq_u32 s3, 1
	s_cbranch_scc1 .Lic2p_t1
	s_cmp_eq_u32 s3, 2
	s_cbranch_scc1 .Lic2p_t2
	s_cmp_eq_u32 s3, 3
	s_cbranch_scc1 .Lic2p_t3
	s_cmp_eq_u32 s3, 4
	s_cbranch_scc1 .Lic2p_t4
	s_cmp_eq_u32 s3, 5
	s_cbranch_scc1 .Lic2p_t5
	s_cmp_eq_u32 s3, 6
	s_cbranch_scc1 .Lic2p_t6
	s_cmp_eq_u32 s3, 7
	s_cbranch_scc1 .Lic2p_t7
	s_cmp_eq_u32 s3, 8
	s_cbranch_scc1 .Lic2p_t8
	s_cmp_eq_u32 s3, 9
	s_cbranch_scc1 .Lic2p_t9

	.amdhsa_kernel _Z7k_layerILi2EEvPKDF16_PKiPKjS3_S3_S1_PKfPDF16_PhS3_S7_Pf
		.amdhsa_group_segment_fixed_size 35584
		.amdhsa_private_segment_fixed_size 0
		.amdhsa_kernarg_size 352
		.amdhsa_user_sgpr_count 2
		.amdhsa_user_sgpr_dispatch_ptr 0
		.amdhsa_user_sgpr_queue_ptr 0
		.amdhsa_user_sgpr_kernarg_segment_ptr 1
		.amdhsa_user_sgpr_dispatch_id 0
		.amdhsa_user_sgpr_kernarg_preload_length 0
		.amdhsa_user_sgpr_kernarg_preload_offset 0
		.amdhsa_user_sgpr_private_segment_size 0
		.amdhsa_uses_dynamic_stack 0
		.amdhsa_enable_private_segment 0
		.amdhsa_system_sgpr_workgroup_id_x 1
		.amdhsa_system_sgpr_workgroup_id_y 0
		.amdhsa_system_sgpr_workgroup_id_z 0
		.amdhsa_system_sgpr_workgroup_info 0
		.amdhsa_system_vgpr_workitem_id 0
		.amdhsa_next_free_vgpr 105
		.amdhsa_next_free_sgpr 42
		.amdhsa_accum_offset 108
		.amdhsa_reserve_vcc 1
		.amdhsa_float_round_mode_32 0
		.amdhsa_float_round_mode_16_64 0
		.amdhsa_float_denorm_mode_32 3
		.amdhsa_float_denorm_mode_16_64 3
		.amdhsa_dx10_clamp 1
		.amdhsa_ieee_mode 1
		.amdhsa_fp16_overflow 0
		.amdhsa_tg_split 0
		.amdhsa_exception_fp_ieee_invalid_op 0
		.amdhsa_exception_fp_denorm_src 0
		.amdhsa_exception_fp_ieee_div_zero 0
		.amdhsa_exception_fp_ieee_overflow 0
		.amdhsa_exception_fp_ieee_underflow 0
		.amdhsa_exception_fp_ieee_inexact 0
		.amdhsa_exception_int_div_zero 0
	.end_amdhsa_kernel

amdhsa.kernels:
  - .agpr_count:     0
    .args:
      - .actual_access:  read_only
        .address_space:  global
        .offset:         0
        .size:           8
        .value_kind:     global_buffer
      - .actual_access:  read_only
        .address_space:  global
        .offset:         8
        .size:           8
        .value_kind:     global_buffer
      - .actual_access:  read_only
        .address_space:  global
        .offset:         16
        .size:           8
        .value_kind:     global_buffer
      - .actual_access:  read_only
        .address_space:  global
        .offset:         24
        .size:           8
        .value_kind:     global_buffer
      - .actual_access:  read_only
        .address_space:  global
        .offset:         32
        .size:           8
        .value_kind:     global_buffer
      - .actual_access:  read_only
        .address_space:  global
        .offset:         40
        .size:           8
        .value_kind:     global_buffer
      - .actual_access:  read_only
        .address_space:  global
        .offset:         48
        .size:           8
        .value_kind:     global_buffer
      - .actual_access:  read_only
        .address_space:  global
        .offset:         56
        .size:           8
        .value_kind:     global_buffer
      - .actual_access:  read_only
        .address_space:  global
        .offset:         64
        .size:           8
        .value_kind:     global_buffer
      - .actual_access:  read_only
        .address_space:  global
        .offset:         72
        .size:           8
        .value_kind:     global_buffer
      - .actual_access:  read_only
        .address_space:  global
        .offset:         80
        .size:           8
        .value_kind:     global_buffer
      - .actual_access:  read_only
        .address_space:  global
        .offset:         88
        .size:           8
        .value_kind:     global_buffer
      - .actual_access:  write_only
        .address_space:  global
        .offset:         96
        .size:           8
        .value_kind:     global_buffer
      - .actual_access:  write_only
        .address_space:  global
        .offset:         104
        .size:           8
        .value_kind:     global_buffer
      - .actual_access:  write_only
        .address_space:  global
        .offset:         112
        .size:           8
        .value_kind:     global_buffer
      - .actual_access:  write_only
        .address_space:  global
        .offset:         120
        .size:           8
        .value_kind:     global_buffer
      - .actual_access:  write_only
        .address_space:  global
        .offset:         128
        .size:           8
        .value_kind:     global_buffer
      - .actual_access:  write_only
        .address_space:  global
        .offset:         136
        .size:           8
        .value_kind:     global_buffer
      - .actual_access:  write_only
        .address_space:  global
        .offset:         144
        .size:           8
        .value_kind:     global_buffer
      - .actual_access:  write_only
        .address_space:  global
        .offset:         152
        .size:           8
        .value_kind:     global_buffer
      - .actual_access:  write_only
        .address_space:  global
        .offset:         160
        .size:           8
        .value_kind:     global_buffer
    .group_segment_fixed_size: 0
    .kernarg_segment_align: 8
    .kernarg_segment_size: 168
    .language:       OpenCL C
    .language_version:
      - 2
      - 0
    .max_flat_workgroup_size: 1024
    .name:           _Z6k_prepPKiS0_PKfS2_S2_S2_S2_S2_S2_S2_S2_S2_PDF16_S3_S3_PfS4_S4_PjS3_S5_
    .private_segment_fixed_size: 0
    .sgpr_count:     27
    .sgpr_spill_count: 0
    .symbol:         _Z6k_prepPKiS0_PKfS2_S2_S2_S2_S2_S2_S2_S2_S2_PDF16_S3_S3_PfS4_S4_PjS3_S5_.kd
    .uniform_work_group_size: 1
    .uses_dynamic_stack: false
    .vgpr_count:     61
    .vgpr_spill_count: 0
    .wavefront_size: 64
  - .agpr_count:     0
    .args:
      - .actual_access:  read_only
        .address_space:  global
        .offset:         0
        .size:           8
        .value_kind:     global_buffer
      - .actual_access:  read_only
        .address_space:  global
        .offset:         8
        .size:           8
        .value_kind:     global_buffer
      - .actual_access:  read_only
        .address_space:  global
        .offset:         16
        .size:           8
        .value_kind:     global_buffer
      - .actual_access:  write_only
        .address_space:  global
        .offset:         24
        .size:           8
        .value_kind:     global_buffer
      - .actual_access:  write_only
        .address_space:  global
        .offset:         32
        .size:           8
        .value_kind:     global_buffer
      - .actual_access:  write_only
        .address_space:  global
        .offset:         40
        .size:           8
        .value_kind:     global_buffer
      - .actual_access:  read_only
        .address_space:  global
        .offset:         48
        .size:           8
        .value_kind:     global_buffer
      - .actual_access:  read_only
        .address_space:  global
        .offset:         56
        .size:           8
        .value_kind:     global_buffer
      - .actual_access:  read_only
        .address_space:  global
        .offset:         64
        .size:           8
        .value_kind:     global_buffer
      - .actual_access:  read_only
        .address_space:  global
        .offset:         72
        .size:           8
        .value_kind:     global_buffer
      - .actual_access:  read_only
        .address_space:  global
        .offset:         80
        .size:           8
        .value_kind:     global_buffer
      - .actual_access:  read_only
        .address_space:  global
        .offset:         88
        .size:           8
        .value_kind:     global_buffer
      - .actual_access:  read_only
        .address_space:  global
        .offset:         96
        .size:           8
        .value_kind:     global_buffer
      - .actual_access:  read_only
        .address_space:  global
        .offset:         104
        .size:           8
        .value_kind:     global_buffer
      - .actual_access:  read_only
        .address_space:  global
        .offset:         112
        .size:           8
        .value_kind:     global_buffer
      - .actual_access:  read_only
        .address_space:  global
        .offset:         120
        .size:           8
        .value_kind:     global_buffer
      - .actual_access:  read_only
        .address_space:  global
        .offset:         128
        .size:           8
        .value_kind:     global_buffer
      - .actual_access:  write_only
        .address_space:  global
        .offset:         136
        .size:           8
        .value_kind:     global_buffer
      - .actual_access:  write_only
        .address_space:  global
        .offset:         144
        .size:           8
        .value_kind:     global_buffer
      - .actual_access:  write_only
        .address_space:  global
        .offset:         152
        .size:           8
        .value_kind:     global_buffer
      - .actual_access:  write_only
        .address_space:  global
        .offset:         160
        .size:           8
        .value_kind:     global_buffer
      - .actual_access:  write_only
        .address_space:  global
        .offset:         168
        .size:           8
        .value_kind:     global_buffer
    .group_segment_fixed_size: 1696
    .kernarg_segment_align: 8
    .kernarg_segment_size: 176
    .language:       OpenCL C
    .language_version:
      - 2
      - 0
    .max_flat_workgroup_size: 1024
    .name:           _Z11k_localsortPKiS0_S0_PjPtPiPKjPKfS7_S7_S7_S7_S7_S7_S7_S7_S7_PDF16_S8_S8_PfS9_
    .private_segment_fixed_size: 0
    .sgpr_count:     71
    .sgpr_spill_count: 0
    .symbol:         _Z11k_localsortPKiS0_S0_PjPtPiPKjPKfS7_S7_S7_S7_S7_S7_S7_S7_S7_PDF16_S8_S8_PfS9_.kd
    .uniform_work_group_size: 1
    .uses_dynamic_stack: false
    .vgpr_count:     96
    .vgpr_spill_count: 0
    .wavefront_size: 64
  - .agpr_count:     0
    .args:
      - .actual_access:  read_only
        .address_space:  global
        .offset:         0
        .size:           8
        .value_kind:     global_buffer
      - .actual_access:  read_only
        .address_space:  global
        .offset:         8
        .size:           8
        .value_kind:     global_buffer
      - .actual_access:  read_only
        .address_space:  global
        .offset:         16
        .size:           8
        .value_kind:     global_buffer
      - .actual_access:  write_only
        .address_space:  global
        .offset:         24
        .size:           8
        .value_kind:     global_buffer
      - .actual_access:  write_only
        .address_space:  global
        .offset:         32
        .size:           8
        .value_kind:     global_buffer
    .group_segment_fixed_size: 54160
    .kernarg_segment_align: 8
    .kernarg_segment_size: 40
    .language:       OpenCL C
    .language_version:
      - 2
      - 0
    .max_flat_workgroup_size: 1024
    .name:           _Z12k_bucketsortPKjPKtPKiPiPj
    .private_segment_fixed_size: 0
    .sgpr_count:     88
    .sgpr_spill_count: 0
    .symbol:         _Z12k_bucketsortPKjPKtPKiPiPj.kd
    .uniform_work_group_size: 1
    .uses_dynamic_stack: false
    .vgpr_count:     64
    .vgpr_spill_count: 0
    .wavefront_size: 64
  - .agpr_count:     0
    .args:
      - .actual_access:  read_only
        .address_space:  global
        .offset:         0
        .size:           8
        .value_kind:     global_buffer
      - .actual_access:  read_only
        .address_space:  global
        .offset:         8
        .size:           8
        .value_kind:     global_buffer
      - .actual_access:  write_only
        .address_space:  global
        .offset:         16
        .size:           8
        .value_kind:     global_buffer
    .group_segment_fixed_size: 0
    .kernarg_segment_align: 8
    .kernarg_segment_size: 24
    .language:       OpenCL C
    .language_version:
      - 2
      - 0
    .max_flat_workgroup_size: 256
    .name:           _Z7k_finalPKfS0_Pf
    .private_segment_fixed_size: 0
    .sgpr_count:     14
    .sgpr_spill_count: 0
    .symbol:         _Z7k_finalPKfS0_Pf.kd
    .uniform_work_group_size: 1
    .uses_dynamic_stack: false
    .vgpr_count:     10
    .vgpr_spill_count: 0
    .wavefront_size: 64
  - .agpr_count:     0
    .args:
      - .actual_access:  read_only
        .address_space:  global
        .offset:         0
        .size:           8
        .value_kind:     global_buffer
      - .actual_access:  read_only
        .address_space:  global
        .offset:         8
        .size:           8
        .value_kind:     global_buffer
      - .actual_access:  read_only
        .address_space:  global
        .offset:         16
        .size:           8
        .value_kind:     global_buffer
      - .actual_access:  read_only
        .address_space:  global
        .offset:         24
        .size:           8
        .value_kind:     global_buffer
      - .actual_access:  read_only
        .address_space:  global
        .offset:         32
        .size:           8
        .value_kind:     global_buffer
      - .actual_access:  read_only
        .address_space:  global
        .offset:         40
        .size:           8
        .value_kind:     global_buffer
      - .address_space:  global
        .offset:         48
        .size:           8
        .value_kind:     global_buffer
      - .actual_access:  write_only
        .address_space:  global
        .offset:         56
        .size:           8
        .value_kind:     global_buffer
      - .address_space:  global
        .offset:         64
        .size:           8
        .value_kind:     global_buffer
      - .actual_access:  read_only
        .address_space:  global
        .offset:         72
        .size:           8
        .value_kind:     global_buffer
      - .address_space:  global
        .offset:         80
        .size:           8
        .value_kind:     global_buffer
      - .actual_access:  read_only
        .address_space:  global
        .offset:         88
        .size:           8
        .value_kind:     global_buffer
      - .offset:         96
        .size:           4
        .value_kind:     hidden_block_count_x
      - .offset:         100
        .size:           4
        .value_kind:     hidden_block_count_y
      - .offset:         104
        .size:           4
        .value_kind:     hidden_block_count_z
      - .offset:         108
        .size:           2
        .value_kind:     hidden_group_size_x
      - .offset:         110
        .size:           2
        .value_kind:     hidden_group_size_y
      - .offset:         112
        .size:           2
        .value_kind:     hidden_group_size_z
      - .offset:         114
        .size:           2
        .value_kind:     hidden_remainder_x
      - .offset:         116
        .size:           2
        .value_kind:     hidden_remainder_y
      - .offset:         118
        .size:           2
        .value_kind:     hidden_remainder_z
      - .offset:         136
        .size:           8
        .value_kind:     hidden_global_offset_x
      - .offset:         144
        .size:           8
        .value_kind:     hidden_global_offset_y
      - .offset:         152
        .size:           8
        .value_kind:     hidden_global_offset_z
      - .offset:         160
        .size:           2
        .value_kind:     hidden_grid_dims
      - .offset:         216
        .size:           4
        .value_kind:     hidden_dynamic_lds_size
    .group_segment_fixed_size: 35072
    .kernarg_segment_align: 8
    .kernarg_segment_size: 352
    .language:       OpenCL C
    .language_version:
      - 2
      - 0
    .max_flat_workgroup_size: 1024
    .name:           _Z7k_layerILi1EEvPKDF16_PKiPKjS3_S3_S1_PKfPDF16_PhS3_S7_Pf
    .private_segment_fixed_size: 0
    .sgpr_count:     43
    .sgpr_spill_count: 0
    .symbol:         _Z7k_layerILi1EEvPKDF16_PKiPKjS3_S3_S1_PKfPDF16_PhS3_S7_Pf.kd
    .uniform_work_group_size: 1
    .uses_dynamic_stack: false
    .vgpr_count:     117
    .vgpr_spill_count: 0
    .wavefront_size: 64
  - .agpr_count:     0
    .args:
      - .actual_access:  read_only
        .address_space:  global
        .offset:         0
        .size:           8
        .value_kind:     global_buffer
      - .actual_access:  read_only
        .address_space:  global
        .offset:         8
        .size:           8
        .value_kind:     global_buffer
      - .actual_access:  read_only
        .address_space:  global
        .offset:         16
        .size:           8
        .value_kind:     global_buffer
      - .actual_access:  read_only
        .address_space:  global
        .offset:         24
        .size:           8
        .value_kind:     global_buffer
      - .actual_access:  read_only
        .address_space:  global
        .offset:         32
        .size:           8
        .value_kind:     global_buffer
      - .actual_access:  read_only
        .address_space:  global
        .offset:         40
        .size:           8
        .value_kind:     global_buffer
      - .address_space:  global
        .offset:         48
        .size:           8
        .value_kind:     global_buffer
      - .actual_access:  read_only
        .address_space:  global
        .offset:         56
        .size:           8
        .value_kind:     global_buffer
      - .address_space:  global
        .offset:         64
        .size:           8
        .value_kind:     global_buffer
      - .actual_access:  read_only
        .address_space:  global
        .offset:         72
        .size:           8
        .value_kind:     global_buffer
      - .address_space:  global
        .offset:         80
        .size:           8
        .value_kind:     global_buffer
      - .address_space:  global
        .offset:         88
        .size:           8
        .value_kind:     global_buffer
      - .offset:         96
        .size:           4
        .value_kind:     hidden_block_count_x
      - .offset:         100
        .size:           4
        .value_kind:     hidden_block_count_y
      - .offset:         104
        .size:           4
        .value_kind:     hidden_block_count_z
      - .offset:         108
        .size:           2
        .value_kind:     hidden_group_size_x
      - .offset:         110
        .size:           2
        .value_kind:     hidden_group_size_y
      - .offset:         112
        .size:           2
        .value_kind:     hidden_group_size_z
      - .offset:         114
        .size:           2
        .value_kind:     hidden_remainder_x
      - .offset:         116
        .size:           2
        .value_kind:     hidden_remainder_y
      - .offset:         118
        .size:           2
        .value_kind:     hidden_remainder_z
      - .offset:         136
        .size:           8
        .value_kind:     hidden_global_offset_x
      - .offset:         144
        .size:           8
        .value_kind:     hidden_global_offset_y
      - .offset:         152
        .size:           8
        .value_kind:     hidden_global_offset_z
      - .offset:         160
        .size:           2
        .value_kind:     hidden_grid_dims
      - .offset:         216
        .size:           4
        .value_kind:     hidden_dynamic_lds_size
    .group_segment_fixed_size: 35584
    .kernarg_segment_align: 8
    .kernarg_segment_size: 352
    .language:       OpenCL C
    .language_version:
      - 2
      - 0
    .max_flat_workgroup_size: 1024
    .name:           _Z7k_layerILi2EEvPKDF16_PKiPKjS3_S3_S1_PKfPDF16_PhS3_S7_Pf
    .private_segment_fixed_size: 0
    .sgpr_count:     48
    .sgpr_spill_count: 0
    .symbol:         _Z7k_layerILi2EEvPKDF16_PKiPKjS3_S3_S1_PKfPDF16_PhS3_S7_Pf.kd
    .uniform_work_group_size: 1
    .uses_dynamic_stack: false
    .vgpr_count:     105
    .vgpr_spill_count: 0
    .wavefront_size: 64
